# P1 classes with flattened HBM demand: workgroups 0-63 convert their 4 stolen tiles before their GEMM units, 64-127 after; 192-255 convert 12 tiles; 128-191 run 4 GEMM units
# speedup vs baseline: 1.0043x; 1.0043x over previous
; #define LAS __attribute__((address_space(3)))
; template <class T> __device__ __forceinline__ T* opaque_p(T* p) { asm volatile("" : "+s"(p)); return p; }
; __device__ __forceinline__ int tidx(int wid) { int l; asm volatile("v_mbcnt_lo_u32_b32 %0, -1, 0\n\tv_mbcnt_hi_u32_b32 %0, -1, %0" : "=v"(l)); return (wid << 6) + l; }
; __device__ __forceinline__ int opaque_s(int v) { asm volatile("" : "+s"(v)); return v; }
;     __device__ bool next(int i, Unit& u) const {
;         const long L = (long)i * G + c; if (L >= nwg) return false;
;         int wgid = (int)L; { const int q = nwg / NXCD, r = nwg % NXCD, xcd = wgid % NXCD, off = wgid / NXCD; wgid = (xcd < r ? xcd * (q + 1) : r * (q + 1) + (xcd - r) * q) + off; }
;         const int nig = WGM * nN, gid = wgid / nig, fm = gid * WGM, gsz = (nM - fm) < WGM ? (nM - fm) : WGM;
;         u.pm = fm + ((wgid % nig) % gsz); u.pn = (wgid % nig) / gsz; u.aoff = (unsigned)u.pm * atile; u.boff = (unsigned)u.pn * btile; return true;
; __global__ void __launch_bounds__(NTHREADS, 2) hybrid_fwd(Args a) {
;     ...
;         if (PHEN(1) && IN(pb + 0)) for (int rep = 0; rep < NREP(1); ++rep) { unsigned char* ws = opaque_p(a.ws); LAS unsigned char* lds = opaque_p(lds0); const int bid = opaque_s((int)blockIdx.x); const int tid = tidx(wid0), lane = tid & 63, wave = __builtin_amdgcn_readfirstlane(tid >> 6), gw = bid * NWAVES + wave; (void)lane; (void)gw;
;             pg8::Gemm g{ws, (unsigned)WS_XB, (unsigned)(WS_WIN + (size_t)l * DIN * DM), DM / 2, DM / 2, opaque_s(DM / 2)};
;             pg8::GridOrder S; S.init(MTOK, DIN, DM / 2, DM / 2, G, bid);
;             EpiZ E{(bf16_t*)(ws + WS_Z), (const float*)(ws + WS_COS), (const float*)(ws + WS_SIN)};
;             pg8::gemm_phase<EpiZ, pg8::GridOrder, true, true>(lds, g, S, E, wid0);
.Lcg_a:
	s_movk_i32 s2, 0x400
	v_readlane_b32 s1, v255, 7
	v_mbcnt_lo_u32_b32 v172, -1, 0
	v_mbcnt_hi_u32_b32 v172, -1, v172
	s_waitcnt vmcnt(0)
	v_mbcnt_lo_u32_b32 v0, -1, 0
	v_mbcnt_hi_u32_b32 v0, -1, v0
	s_cmpk_lt_i32 s21, 0x280
	v_add_u32_e32 v173, s78, v172
	v_add_u32_e32 v1, s78, v0
	v_readfirstlane_b32 s20, v173
	s_cselect_b64 s[0:1], -1, 0
	v_readlane_b32 s6, v255, 61
	s_nop 0
	s_cmp_lg_u32 s6, 0
	s_cbranch_scc1 .Lcg_nodiv
	s_cmp_eq_u32 s66, 3
	s_cbranch_scc1 .Lcg_nodiv
	s_cmpk_lt_i32 s21, 0x40
	s_cbranch_scc0 .Lcg_d2
	v_writelane_b32 v255, 5, 61
	s_branch .LBB0_208
.Lcg_d2:
	s_cmpk_lt_i32 s21, 0xc0
	s_cbranch_scc1 .Lcg_nodiv
	v_writelane_b32 v255, 3, 61
	s_branch .LBB0_208

; __global__ void __launch_bounds__(NTHREADS, 2) hybrid_fwd(Args a) {
;     ...
;             if (l + 1 < NLAYER && G == 256 && bid >= 128)
;                 f8_convert<true>(a, lds, ws, l + 1, 0, 0, 2, (unsigned*)(ws + WS_CTL) + CW_TICK + 64 * (l + 1), tid, lane, wave);
.LBB0_208:
	v_readlane_b32 s0, v255, 61
	s_nop 0
	s_cmp_eq_u32 s0, 1
	s_cbranch_scc1 .Lcg_skipc
	s_cmp_eq_u32 s0, 6
	s_cbranch_scc1 .Lcg_skipc
	s_cmp_eq_u32 s0, 5
	s_cbranch_scc0 .Lcg_n5
	s_movk_i32 s21, 0x100
	s_branch .Lcg_208
.Lcg_n5:
	s_cmp_eq_u32 s0, 3
	s_cbranch_scc1 .Lcg_208
	s_cmp_eq_u32 s66, 3
	s_cbranch_scc1 .Lcg_208
	s_cmpk_gt_i32 s21, 0x7f
	s_cbranch_scc1 .Lcg_skipc
	s_movk_i32 s21, 0x100
	s_branch .Lcg_208

; #define LAS __attribute__((address_space(3)))
; template <bool STEAL>
; __device__ __forceinline__ void f8_convert(const Args& a, LAS unsigned char* lds, unsigned char* ws, int l, int first, int stride, int quota, unsigned* ticket, int tid, int lane, int wave) {
;     ...
;     while (k < F8_TILES_PER_LAYER) {
;         LAS unsigned char* buf = lds + (n & 1) * 65536;
;         if constexpr (STEAL) { if (tid == 0) word[(n + 1) & 1] = (n + 1 < quota) ? (int)__hip_atomic_fetch_add(ticket, 1u, __ATOMIC_RELAXED, __HIP_MEMORY_SCOPE_AGENT) : F8_TILES_PER_LAYER; }
.LBB0_247:
	s_and_saveexec_b64 s[2:3], s[0:1]
	s_xor_b64 s[2:3], exec, s[2:3]
	s_and_b32 s4, s35, 1
	s_or_saveexec_b64 s[2:3], s[2:3]
	v_mov_b32_e32 v152, s4
	s_xor_b64 exec, exec, s[2:3]
	s_cbranch_execz .LBB0_253
	v_readlane_b32 s4, v255, 61
	s_nop 0
	s_cmp_eq_u32 s4, 3
	s_cselect_b32 s4, 11, 3
	s_cmp_gt_u32 s35, s4
	v_mov_b32_e32 v152, 0x6e0
	s_cbranch_scc1 .LBB0_252
	v_mov_b64_e32 v[152:153], s[6:7]
	flat_atomic_add v152, v[152:153], v206 sc0

; #define LAS __attribute__((address_space(3)))
; template <class T> __device__ __forceinline__ T* opaque_p(T* p) { asm volatile("" : "+s"(p)); return p; }
; __device__ __forceinline__ int tidx(int wid) { int l; asm volatile("v_mbcnt_lo_u32_b32 %0, -1, 0\n\tv_mbcnt_hi_u32_b32 %0, -1, %0" : "=v"(l)); return (wid << 6) + l; }
; __device__ __forceinline__ int opaque_s(int v) { asm volatile("" : "+s"(v)); return v; }
; __global__ void __launch_bounds__(NTHREADS, 2) hybrid_fwd(Args a) {
;     ...
;         if (PHEN(1) && IN(pb + 0)) for (int rep = 0; rep < NREP(1); ++rep) { unsigned char* ws = opaque_p(a.ws); LAS unsigned char* lds = opaque_p(lds0); const int bid = opaque_s((int)blockIdx.x); const int tid = tidx(wid0), lane = tid & 63, wave = __builtin_amdgcn_readfirstlane(tid >> 6), gw = bid * NWAVES + wave; (void)lane; (void)gw;
;             pg8::Gemm g{ws, (unsigned)WS_XB, (unsigned)(WS_WIN + (size_t)l * DIN * DM), DM / 2, DM / 2, opaque_s(DM / 2)};
;             pg8::GridOrder S; S.init(MTOK, DIN, DM / 2, DM / 2, G, bid);
;             EpiZ E{(bf16_t*)(ws + WS_Z), (const float*)(ws + WS_COS), (const float*)(ws + WS_SIN)};
;             pg8::gemm_phase<EpiZ, pg8::GridOrder, true, true>(lds, g, S, E, wid0);
;             if (l + 1 < NLAYER && G == 256 && bid >= 128)
;                 f8_convert<true>(a, lds, ws, l + 1, 0, 0, 2, (unsigned*)(ws + WS_CTL) + CW_TICK + 64 * (l + 1), tid, lane, wave);
;         }
.LBB0_284:
	v_readlane_b32 s36, v255, 61
	s_nop 0
	s_cmp_eq_u32 s36, 0
	s_cbranch_scc1 .Lcg_first
	s_cmp_eq_u32 s36, 5
	s_cbranch_scc0 .Lcg_rst
	v_writelane_b32 v255, 6, 61
	s_waitcnt vmcnt(0) lgkmcnt(0)
	s_barrier
	s_branch .Lcg_setup
.Lcg_rst:
	v_writelane_b32 v255, 0, 61
	s_branch .Lcg_x
